# NSA tile loop: QK and PV fragment LDS reads issued ahead (10 / 3 deep) on top of the static younger-half priority
# speedup vs baseline: 1.0104x; 1.0007x over previous
.LBB0_914:
	s_mul_i32 s18, s24, 0x9400
	s_add_i32 s27, s18, 0
	v_add3_u32 v3, s27, v181, v180
	ds_read_b128 v[84:87], v3 offset:8704
	ds_read_b128 v[68:71], v3
	ds_read_b128 v[100:103], v3 offset:32
	ds_read_b128 v[104:107], v3 offset:8736
	ds_read_b128 v[108:111], v3 offset:64
	ds_read_b128 v[112:115], v3 offset:8768
	ds_read_b128 v[116:119], v3 offset:96
	ds_read_b128 v[120:123], v3 offset:8800
	ds_read_b128 v[124:127], v3 offset:128
	ds_read_b128 v[128:131], v3 offset:8832
	s_mov_b64 s[18:19], -1
	s_waitcnt lgkmcnt(9)
	v_mfma_f32_32x32x16_bf16 v[84:99], v[84:87], v[132:135], 0
	s_and_b64 vcc, exec, s[0:1]
	s_waitcnt lgkmcnt(8)
	v_mfma_f32_32x32x16_bf16 v[68:83], v[68:71], v[132:135], 0
	s_waitcnt lgkmcnt(7)
	v_mfma_f32_32x32x16_bf16 v[68:83], v[100:103], v[140:143], v[68:83]
	s_waitcnt lgkmcnt(6)
	v_mfma_f32_32x32x16_bf16 v[84:99], v[104:107], v[140:143], v[84:99]
	ds_read_b128 v[100:103], v3 offset:160
	ds_read_b128 v[104:107], v3 offset:8864
	s_waitcnt lgkmcnt(7)
	v_mfma_f32_32x32x16_bf16 v[68:83], v[108:111], v[148:151], v[68:83]
	s_waitcnt lgkmcnt(6)
	v_mfma_f32_32x32x16_bf16 v[84:99], v[112:115], v[148:151], v[84:99]
	ds_read_b128 v[108:111], v3 offset:192
	ds_read_b128 v[112:115], v3 offset:8896
	s_waitcnt lgkmcnt(7)
	v_mfma_f32_32x32x16_bf16 v[68:83], v[116:119], v[156:159], v[68:83]
	s_waitcnt lgkmcnt(6)
	v_mfma_f32_32x32x16_bf16 v[84:99], v[120:123], v[156:159], v[84:99]
	ds_read_b128 v[116:119], v3 offset:224
	ds_read_b128 v[120:123], v3 offset:8928
	v_mov_b32_e32 v3, v199
	s_waitcnt lgkmcnt(7)
	v_mfma_f32_32x32x16_bf16 v[68:83], v[124:127], v[136:139], v[68:83]
	s_waitcnt lgkmcnt(6)
	v_mfma_f32_32x32x16_bf16 v[84:99], v[128:131], v[136:139], v[84:99]
	s_waitcnt lgkmcnt(5)
	v_mfma_f32_32x32x16_bf16 v[68:83], v[100:103], v[144:147], v[68:83]
	s_waitcnt lgkmcnt(4)
	v_mfma_f32_32x32x16_bf16 v[84:99], v[104:107], v[144:147], v[84:99]
	s_waitcnt lgkmcnt(3)
	v_mfma_f32_32x32x16_bf16 v[68:83], v[108:111], v[152:155], v[68:83]
	s_waitcnt lgkmcnt(2)
	v_mfma_f32_32x32x16_bf16 v[84:99], v[112:115], v[152:155], v[84:99]
	s_waitcnt lgkmcnt(1)
	v_mfma_f32_32x32x16_bf16 v[68:83], v[116:119], v[160:163], v[68:83]
	s_waitcnt lgkmcnt(0)
	v_mfma_f32_32x32x16_bf16 v[84:99], v[120:123], v[160:163], v[84:99]
	s_cbranch_vccz .LBB0_922
	s_cmp_lg_u32 s22, s84
	s_cbranch_scc0 .LBB0_919
	s_nop 6
	v_mov_b64_e32 v[130:131], v[82:83]
	s_nop 0
	v_mov_b64_e32 v[114:115], v[98:99]
	s_cmp_lg_u32 s22, s5
	v_mov_b64_e32 v[128:129], v[80:81]
	v_mov_b64_e32 v[126:127], v[78:79]
	v_mov_b64_e32 v[124:125], v[76:77]
	v_mov_b64_e32 v[122:123], v[74:75]
	v_mov_b64_e32 v[120:121], v[72:73]
	v_mov_b64_e32 v[118:119], v[70:71]
	v_mov_b64_e32 v[116:117], v[68:69]
	v_mov_b64_e32 v[112:113], v[96:97]
	v_mov_b64_e32 v[110:111], v[94:95]
	v_mov_b64_e32 v[108:109], v[92:93]
	v_mov_b64_e32 v[106:107], v[90:91]
	v_mov_b64_e32 v[104:105], v[88:89]
	v_mov_b64_e32 v[102:103], v[86:87]
	v_mov_b64_e32 v[100:101], v[84:85]
	s_cbranch_scc1 .LBB0_918
	v_cmp_gt_i32_e32 vcc, v209, v3
	s_nop 1
	v_cndmask_b32_e32 v116, v194, v68, vcc
	v_cmp_gt_i32_e32 vcc, v210, v3
	s_nop 1
	v_cndmask_b32_e32 v100, v194, v84, vcc
	v_cmp_ge_i32_e32 vcc, v209, v3
	s_nop 1
	v_cndmask_b32_e32 v117, v194, v69, vcc
	v_cmp_gt_i32_e32 vcc, v211, v3
	s_nop 1
	v_cndmask_b32_e32 v101, v194, v85, vcc
	v_cmp_gt_i32_e32 vcc, v212, v3
	s_nop 1
	v_cndmask_b32_e32 v118, v194, v70, vcc
	v_cmp_gt_i32_e32 vcc, v213, v3
	s_nop 1
	v_cndmask_b32_e32 v102, v194, v86, vcc
	v_cmp_gt_i32_e32 vcc, v214, v3
	s_nop 1
	v_cndmask_b32_e32 v119, v194, v71, vcc
	v_cmp_gt_i32_e32 vcc, v215, v3
	s_nop 1
	v_cndmask_b32_e32 v103, v194, v87, vcc
	v_cmp_gt_i32_e32 vcc, v216, v3
	s_nop 1
	v_cndmask_b32_e32 v120, v194, v72, vcc
	v_cmp_gt_i32_e32 vcc, v217, v3
	s_nop 1
	v_cndmask_b32_e32 v104, v194, v88, vcc
	v_cmp_gt_i32_e32 vcc, v218, v3
	s_nop 1
	v_cndmask_b32_e32 v121, v194, v73, vcc
	v_cmp_gt_i32_e32 vcc, v219, v3
	s_nop 1
	v_cndmask_b32_e32 v105, v194, v89, vcc
	v_cmp_gt_i32_e32 vcc, v220, v3
	s_nop 1
	v_cndmask_b32_e32 v122, v194, v74, vcc
	v_cmp_gt_i32_e32 vcc, v221, v3
	s_nop 1
	v_cndmask_b32_e32 v106, v194, v90, vcc
	v_cmp_gt_i32_e32 vcc, v222, v3
	s_nop 1
	v_cndmask_b32_e32 v123, v194, v75, vcc
	v_cmp_gt_i32_e32 vcc, v223, v3
	s_nop 1
	v_cndmask_b32_e32 v107, v194, v91, vcc
	v_cmp_gt_i32_e32 vcc, v224, v3
	s_nop 1
	v_cndmask_b32_e32 v124, v194, v76, vcc
	v_cmp_gt_i32_e32 vcc, v225, v3
	s_nop 1
	v_cndmask_b32_e32 v108, v194, v92, vcc
	v_cmp_gt_i32_e32 vcc, v226, v3
	s_nop 1
	v_cndmask_b32_e32 v125, v194, v77, vcc
	v_cmp_gt_i32_e32 vcc, v227, v3
	s_nop 1
	v_cndmask_b32_e32 v109, v194, v93, vcc
	v_cmp_gt_i32_e32 vcc, v229, v3
	s_nop 1
	v_cndmask_b32_e32 v126, v194, v78, vcc
	v_cmp_gt_i32_e32 vcc, v230, v3
	s_nop 1
	v_cndmask_b32_e32 v110, v194, v94, vcc
	v_cmp_gt_i32_e32 vcc, v231, v3
	s_nop 1
	v_cndmask_b32_e32 v127, v194, v79, vcc
	v_cmp_gt_i32_e32 vcc, v232, v3
	s_nop 1
	v_cndmask_b32_e32 v111, v194, v95, vcc
	v_cmp_gt_i32_e32 vcc, v233, v3
	s_nop 1
	v_cndmask_b32_e32 v128, v194, v80, vcc
	v_cmp_gt_i32_e32 vcc, v234, v3
	s_nop 1
	v_cndmask_b32_e32 v112, v194, v96, vcc
	v_cmp_gt_i32_e32 vcc, v235, v3
	s_nop 1
	v_cndmask_b32_e32 v129, v194, v81, vcc
	v_cmp_gt_i32_e32 vcc, v236, v3
	s_nop 1
	v_cndmask_b32_e32 v113, v194, v97, vcc
	v_cmp_gt_i32_e32 vcc, v237, v3
	s_nop 1
	v_cndmask_b32_e32 v130, v194, v82, vcc
	v_cmp_gt_i32_e32 vcc, v238, v3
	s_nop 1
	v_cndmask_b32_e32 v114, v194, v98, vcc
	v_cmp_gt_i32_e32 vcc, v239, v3
	s_nop 1
	v_cndmask_b32_e32 v131, v194, v83, vcc
	v_cmp_gt_i32_e32 vcc, v240, v3
	s_nop 1
	v_cndmask_b32_e32 v115, v194, v99, vcc
